# g8: g7 + mLSTM k2 loop LDS reads issued ahead of their MFMAs (one extra fragment quad), decay arithmetic grouped
# speedup vs baseline: 1.0122x; 1.0013x over previous
.LBB0_267:
	v_add_u32_e32 v104, 0, v236
	ds_read_b128 v[238:241], v104
	ds_read_b128 v[242:245], v104 offset:64
	ds_read_b128 v[248:251], v104 offset:128
	v_add_u32_e32 v105, 0, v230
	v_add_u32_e32 v103, 0x22000, v105
	s_cmp_lt_u32 s48, s82
	s_cselect_b64 vcc, -1, 0
	s_cmp_eq_u32 s48, s82
	s_cselect_b64 s[0:1], -1, 0
	s_and_b64 s[30:31], s[20:21], s[0:1]
	s_waitcnt lgkmcnt(2)
	v_mfma_f32_16x16x32_bf16 v[238:241], v[238:241], v[78:81], 0
	s_or_b64 s[30:31], vcc, s[30:31]
	v_add_u32_e32 v230, 0x80, v230
	v_add_u32_e32 v236, 0x2200, v236
	s_waitcnt lgkmcnt(1)
	v_mfma_f32_16x16x32_bf16 v[238:241], v[242:245], v[70:73], v[238:241]
	ds_read_b128 v[242:245], v104 offset:192
	s_waitcnt lgkmcnt(1)
	v_mfma_f32_16x16x32_bf16 v[238:241], v[248:251], v[66:69], v[238:241]
	ds_read_b128 v[248:251], v103
	s_waitcnt lgkmcnt(1)
	v_mfma_f32_16x16x32_bf16 v[238:241], v[242:245], v[82:85], v[238:241]
	ds_read_b128 v[242:245], v104 offset:4352
	s_waitcnt lgkmcnt(1)
	v_sub_f32_e32 v248, v248, v231
	v_sub_f32_e32 v249, v249, v231
	v_sub_f32_e32 v250, v250, v231
	v_sub_f32_e32 v251, v251, v231
	v_mul_f32_e32 v248, 0x3fb8aa3b, v248
	v_mul_f32_e32 v249, 0x3fb8aa3b, v249
	v_mul_f32_e32 v250, 0x3fb8aa3b, v250
	v_mul_f32_e32 v251, 0x3fb8aa3b, v251
	v_exp_f32_e32 v248, v248
	v_exp_f32_e32 v249, v249
	v_exp_f32_e32 v250, v250
	v_exp_f32_e32 v251, v251
	v_mul_f32_e32 v238, v238, v248
	v_mul_f32_e32 v239, v239, v249
	v_mul_f32_e32 v240, v240, v250
	v_mul_f32_e32 v241, v241, v251
	v_mul_f32_e32 v238, 0x3db504f3, v238
	v_mul_f32_e32 v239, 0x3db504f3, v239
	v_mul_f32_e32 v240, 0x3db504f3, v240
	v_mul_f32_e32 v241, 0x3db504f3, v241
	v_cndmask_b32_e64 v237, v238, 0, s[18:19]
	v_cndmask_b32_e64 v247, v240, 0, s[22:23]
	v_cndmask_b32_e64 v103, v241, 0, s[24:25]
	v_cndmask_b32_e64 v237, 0, v237, s[0:1]
	v_cndmask_b32_e64 v247, 0, v247, s[0:1]
	v_cndmask_b32_e64 v103, 0, v103, s[0:1]
	v_cndmask_b32_e32 v238, v237, v238, vcc
	v_cndmask_b32_e32 v240, v247, v240, vcc
	v_cndmask_b32_e32 v241, v103, v241, vcc
	v_cndmask_b32_e64 v239, 0, v239, s[30:31]
	v_add_f32_e32 v237, v239, v238
	v_add_f32_e32 v247, v240, v241
	v_add_f32_e32 v237, v237, v247
	v_add_f32_e32 v246, v102, v237
	v_cvt_pk_bf16_f32 v102, v238, v239
	s_nop 1
	v_cvt_pk_bf16_f32 v103, v240, v241
	s_nop 1
	ds_read_b128 v[238:241], v104 offset:4416
	ds_read_b128 v[248:251], v104 offset:4480
	s_add_i32 s0, s48, 1
	s_cmp_lt_u32 s0, s82
	s_cselect_b64 vcc, -1, 0
	s_cmp_eq_u32 s0, s82
	s_cselect_b64 s[0:1], -1, 0
	s_and_b64 s[30:31], s[20:21], s[0:1]
	s_or_b64 s[30:31], vcc, s[30:31]
	s_add_i32 s48, s48, 2
	s_waitcnt lgkmcnt(2)
	v_mfma_f32_16x16x32_bf16 v[242:245], v[242:245], v[78:81], 0
	s_waitcnt lgkmcnt(1)
	v_mfma_f32_16x16x32_bf16 v[242:245], v[238:241], v[70:73], v[242:245]
	ds_read_b128 v[238:241], v104 offset:4544
	s_waitcnt lgkmcnt(1)
	v_mfma_f32_16x16x32_bf16 v[242:245], v[248:251], v[66:69], v[242:245]
	v_add_u32_e32 v104, 0x22040, v105
	ds_read_b128 v[248:251], v104
	s_waitcnt lgkmcnt(1)
	v_mfma_f32_16x16x32_bf16 v[242:245], v[238:241], v[82:85], v[242:245]
	v_add_u32_e32 v237, 0, v232
	ds_read_b64 v[238:239], v237
	v_add_u32_e32 v237, 0, v233
	ds_read_b64 v[240:241], v237
	s_waitcnt lgkmcnt(2)
	v_sub_f32_e32 v248, v248, v231
	v_sub_f32_e32 v249, v249, v231
	v_sub_f32_e32 v250, v250, v231
	v_sub_f32_e32 v251, v251, v231
	v_mul_f32_e32 v248, 0x3fb8aa3b, v248
	v_mul_f32_e32 v249, 0x3fb8aa3b, v249
	v_mul_f32_e32 v250, 0x3fb8aa3b, v250
	v_mul_f32_e32 v251, 0x3fb8aa3b, v251
	v_exp_f32_e32 v248, v248
	v_exp_f32_e32 v249, v249
	v_exp_f32_e32 v250, v250
	v_exp_f32_e32 v251, v251
	v_mul_f32_e32 v242, v242, v248
	v_mul_f32_e32 v243, v243, v249
	v_mul_f32_e32 v244, v244, v250
	v_mul_f32_e32 v245, v245, v251
	v_mul_f32_e32 v242, 0x3db504f3, v242
	v_mul_f32_e32 v243, 0x3db504f3, v243
	v_mul_f32_e32 v244, 0x3db504f3, v244
	v_mul_f32_e32 v245, 0x3db504f3, v245
	v_cndmask_b32_e64 v237, v242, 0, s[18:19]
	v_cndmask_b32_e64 v247, v244, 0, s[22:23]
	v_cndmask_b32_e64 v104, v245, 0, s[24:25]
	v_cndmask_b32_e64 v237, 0, v237, s[0:1]
	v_cndmask_b32_e64 v247, 0, v247, s[0:1]
	v_cndmask_b32_e64 v104, 0, v104, s[0:1]
	v_cndmask_b32_e32 v242, v237, v242, vcc
	v_cndmask_b32_e32 v244, v247, v244, vcc
	v_cndmask_b32_e32 v245, v104, v245, vcc
	v_cndmask_b32_e64 v243, 0, v243, s[30:31]
	v_add_f32_e32 v237, v243, v242
	v_add_f32_e32 v247, v244, v245
	v_add_f32_e32 v247, v237, v247
	v_cvt_pk_bf16_f32 v104, v242, v243
	s_nop 1
	v_cvt_pk_bf16_f32 v105, v244, v245
	s_nop 1
	v_add_u32_e32 v237, 0, v234
	ds_read_b64 v[242:243], v237
	v_add_u32_e32 v237, 0, v235
	ds_read_b64 v[244:245], v237
	s_xor_b32 s0, s4, 64
	v_add_u32_e32 v237, s0, v170
	ds_read_b64 v[248:249], v237 offset:8704
	v_add_u32_e32 v237, s0, v171
	ds_read_b64 v[250:251], v237 offset:8704
	s_waitcnt lgkmcnt(4)
	v_mfma_f32_16x16x32_bf16 v[86:89], v[102:105], v[238:241], v[86:89]
	v_add_u32_e32 v237, s0, v172
	ds_read_b64 v[238:239], v237 offset:13056
	v_add_u32_e32 v237, s0, v173
	ds_read_b64 v[240:241], v237 offset:13056
	s_waitcnt lgkmcnt(4)
	v_mfma_f32_16x16x32_bf16 v[90:93], v[102:105], v[242:245], v[90:93]
	s_waitcnt lgkmcnt(2)
	v_mfma_f32_16x16x32_bf16 v[94:97], v[102:105], v[248:251], v[94:97]
	s_waitcnt lgkmcnt(0)
	v_mfma_f32_16x16x32_bf16 v[98:101], v[102:105], v[238:241], v[98:101]
	s_add_i32 s4, s4, 64
	v_add_f32_e32 v102, v246, v247
	v_add_u32_e32 v235, 64, v235
	v_add_u32_e32 v234, 64, v234
	v_add_u32_e32 v233, 64, v233
	v_add_u32_e32 v232, 64, v232
	s_cmp_eq_u32 s87, s48
	s_cbranch_scc0 .LBB0_267
	ds_read_b128 v[230:233], v191
	v_lshlrev_b32_e32 v104, 16, v78
	v_and_b32_e32 v105, 0xffff0000, v78
	v_lshlrev_b32_e32 v234, 16, v79
	v_and_b32_e32 v235, 0xffff0000, v79
	v_lshlrev_b32_e32 v236, 16, v80
	v_and_b32_e32 v237, 0xffff0000, v80
	v_lshlrev_b32_e32 v238, 16, v81
	v_and_b32_e32 v239, 0xffff0000, v81
	ds_read_b128 v[78:81], v191 offset:16
	s_waitcnt lgkmcnt(1)
	v_mul_f32_e32 v105, v231, v105
	v_fmac_f32_e32 v105, v230, v104
	v_fmac_f32_e32 v105, v232, v234
	v_fmac_f32_e32 v105, v233, v235
	s_waitcnt lgkmcnt(0)
	v_fmac_f32_e32 v105, v78, v236
	v_fmac_f32_e32 v105, v79, v237
	v_fmac_f32_e32 v105, v80, v238
	v_fmac_f32_e32 v105, v81, v239
	ds_read_b128 v[78:81], v191 offset:128
	v_add_f32_e32 v104, 0, v105
	v_lshlrev_b32_e32 v105, 16, v70
	v_and_b32_e32 v230, 0xffff0000, v70
	v_lshlrev_b32_e32 v231, 16, v71
	v_and_b32_e32 v232, 0xffff0000, v71
	v_lshlrev_b32_e32 v233, 16, v72
	v_and_b32_e32 v234, 0xffff0000, v72
	v_lshlrev_b32_e32 v235, 16, v73
	v_and_b32_e32 v236, 0xffff0000, v73
	ds_read_b128 v[70:73], v191 offset:144
	s_waitcnt lgkmcnt(1)
	v_mul_f32_e32 v79, v79, v230
	v_fmac_f32_e32 v79, v78, v105
	v_fmac_f32_e32 v79, v80, v231
	v_fmac_f32_e32 v79, v81, v232
	s_waitcnt lgkmcnt(0)
	v_fmac_f32_e32 v79, v70, v233
	v_fmac_f32_e32 v79, v71, v234
	v_fmac_f32_e32 v79, v72, v235
	v_fmac_f32_e32 v79, v73, v236
	ds_read_b128 v[70:73], v191 offset:256
	v_add_f32_e32 v78, v104, v79
	v_lshlrev_b32_e32 v79, 16, v66
	v_and_b32_e32 v80, 0xffff0000, v66
	v_lshlrev_b32_e32 v81, 16, v67
	v_and_b32_e32 v104, 0xffff0000, v67
	v_lshlrev_b32_e32 v105, 16, v68
	v_and_b32_e32 v230, 0xffff0000, v68
	v_lshlrev_b32_e32 v231, 16, v69
	v_and_b32_e32 v232, 0xffff0000, v69
	ds_read_b128 v[66:69], v191 offset:272
	s_waitcnt lgkmcnt(1)
	v_mul_f32_e32 v71, v71, v80
	v_fmac_f32_e32 v71, v70, v79
	v_fmac_f32_e32 v71, v72, v81
	v_fmac_f32_e32 v71, v73, v104
	s_waitcnt lgkmcnt(0)
	v_fmac_f32_e32 v71, v66, v105
	v_fmac_f32_e32 v71, v67, v230
	v_fmac_f32_e32 v71, v68, v231
	v_fmac_f32_e32 v71, v69, v232
	ds_read_b128 v[66:69], v191 offset:384
	v_add_f32_e32 v78, v78, v71
	v_and_b32_e32 v80, 0xffff0000, v82
	ds_read_b128 v[70:73], v191 offset:400
	v_lshlrev_b32_e32 v79, 16, v82
	s_waitcnt lgkmcnt(1)
	v_mul_f32_e32 v67, v67, v80
	v_lshlrev_b32_e32 v81, 16, v83
	v_fmac_f32_e32 v67, v66, v79
	v_and_b32_e32 v82, 0xffff0000, v83
	v_fmac_f32_e32 v67, v68, v81
	v_lshlrev_b32_e32 v83, 16, v84
	v_fmac_f32_e32 v67, v69, v82
	v_and_b32_e32 v84, 0xffff0000, v84
	s_waitcnt lgkmcnt(0)
	v_fmac_f32_e32 v67, v70, v83
	v_lshlrev_b32_e32 v104, 16, v85
	v_fmac_f32_e32 v67, v71, v84
	v_and_b32_e32 v85, 0xffff0000, v85
	v_fmac_f32_e32 v67, v72, v104
	v_fmac_f32_e32 v67, v73, v85
	v_add_f32_e32 v68, v78, v67
	ds_bpermute_b32 v103, v221, v102
	ds_bpermute_b32 v69, v221, v68
	s_waitcnt lgkmcnt(1)
	v_add_f32_e32 v66, v102, v103
	s_waitcnt lgkmcnt(0)
	v_add_f32_e32 v68, v68, v69
	ds_bpermute_b32 v67, v222, v66
	ds_bpermute_b32 v69, v222, v68
	s_and_saveexec_b64 s[0:1], s[14:15]
	s_cbranch_execz .LBB0_270
	s_waitcnt lgkmcnt(1)
	v_add_f32_e32 v66, v66, v67
	s_waitcnt lgkmcnt(0)
	v_add_f32_e32 v67, v68, v69
	ds_write_b32 v178, v66
	ds_write_b32 v177, v67 offset:64
